# P6 projection stores write-through (sc0 sc1 nt): nothing dirty left for the release fence of the following grid barrier
# speedup vs baseline: 1.0074x; 1.0074x over previous
.LBB0_974:
	s_nop 0
	v_cndmask_b32_e64 v4, 0, 1, s[4:5]
	v_cmp_ne_u32_e64 s[38:39], 1, v4
	v_or_b32_e32 v4, s13, v180
	v_mad_u32_u24 v228, v4, s33, v2
	ds_read_b128 v[4:7], v228
	ds_read_b128 v[196:199], v228 offset:32
	ds_read_b128 v[204:207], v228 offset:64
	ds_read_b128 v[208:211], v228 offset:96
	ds_read_b128 v[212:215], v228 offset:128
	ds_read_b128 v[216:219], v228 offset:160
	ds_read_b128 v[220:223], v228 offset:192
	ds_read_b128 v[224:227], v228 offset:224
	s_waitcnt lgkmcnt(7)
	v_mfma_f32_32x32x16_bf16 v[20:35], v[36:39], v[4:7], 0
	v_mfma_f32_32x32x16_bf16 v[4:19], v[100:103], v[4:7], 0
	s_waitcnt lgkmcnt(6)
	v_mfma_f32_32x32x16_bf16 v[20:35], v[40:43], v[196:199], v[20:35]
	v_mfma_f32_32x32x16_bf16 v[4:19], v[104:107], v[196:199], v[4:19]
	s_waitcnt lgkmcnt(5)
	v_mfma_f32_32x32x16_bf16 v[20:35], v[44:47], v[204:207], v[20:35]
	v_mfma_f32_32x32x16_bf16 v[4:19], v[108:111], v[204:207], v[4:19]
	s_waitcnt lgkmcnt(4)
	v_mfma_f32_32x32x16_bf16 v[20:35], v[48:51], v[208:211], v[20:35]
	v_mfma_f32_32x32x16_bf16 v[4:19], v[112:115], v[208:211], v[4:19]
	s_waitcnt lgkmcnt(3)
	v_mfma_f32_32x32x16_bf16 v[20:35], v[52:55], v[212:215], v[20:35]
	v_mfma_f32_32x32x16_bf16 v[4:19], v[116:119], v[212:215], v[4:19]
	s_waitcnt lgkmcnt(2)
	v_mfma_f32_32x32x16_bf16 v[20:35], v[56:59], v[216:219], v[20:35]
	v_mfma_f32_32x32x16_bf16 v[4:19], v[120:123], v[216:219], v[4:19]
	s_waitcnt lgkmcnt(1)
	v_mfma_f32_32x32x16_bf16 v[20:35], v[60:63], v[220:223], v[20:35]
	v_mfma_f32_32x32x16_bf16 v[4:19], v[124:127], v[220:223], v[4:19]
	s_waitcnt lgkmcnt(0)
	v_mfma_f32_32x32x16_bf16 v[20:35], v[64:67], v[224:227], v[20:35]
	v_mfma_f32_32x32x16_bf16 v[4:19], v[128:131], v[224:227], v[4:19]
	ds_read_b128 v[196:199], v228 offset:256
	ds_read_b128 v[204:207], v228 offset:288
	ds_read_b128 v[208:211], v228 offset:320
	ds_read_b128 v[212:215], v228 offset:352
	ds_read_b128 v[216:219], v228 offset:384
	ds_read_b128 v[220:223], v228 offset:416
	ds_read_b128 v[224:227], v228 offset:448
	ds_read_b128 v[228:231], v228 offset:480
	s_waitcnt lgkmcnt(7)
	v_mfma_f32_32x32x16_bf16 v[20:35], v[68:71], v[196:199], v[20:35]
	s_mov_b64 s[4:5], 0
	v_mfma_f32_32x32x16_bf16 v[4:19], v[132:135], v[196:199], v[4:19]
	v_or_b32_e32 v196, s13, v194
	v_mov_b32_e32 v197, v195
	s_mov_b32 s13, 32
	s_waitcnt lgkmcnt(6)
	v_mfma_f32_32x32x16_bf16 v[20:35], v[72:75], v[204:207], v[20:35]
	v_mfma_f32_32x32x16_bf16 v[4:19], v[136:139], v[204:207], v[4:19]
	s_waitcnt lgkmcnt(5)
	v_mfma_f32_32x32x16_bf16 v[20:35], v[76:79], v[208:211], v[20:35]
	v_mfma_f32_32x32x16_bf16 v[4:19], v[140:143], v[208:211], v[4:19]
	s_waitcnt lgkmcnt(4)
	v_mfma_f32_32x32x16_bf16 v[20:35], v[80:83], v[212:215], v[20:35]
	v_mfma_f32_32x32x16_bf16 v[4:19], v[144:147], v[212:215], v[4:19]
	s_waitcnt lgkmcnt(3)
	v_mfma_f32_32x32x16_bf16 v[20:35], v[84:87], v[216:219], v[20:35]
	v_mfma_f32_32x32x16_bf16 v[4:19], v[148:151], v[216:219], v[4:19]
	s_waitcnt lgkmcnt(2)
	v_mfma_f32_32x32x16_bf16 v[20:35], v[88:91], v[220:223], v[20:35]
	v_mfma_f32_32x32x16_bf16 v[4:19], v[152:155], v[220:223], v[4:19]
	s_waitcnt lgkmcnt(1)
	v_mfma_f32_32x32x16_bf16 v[20:35], v[92:95], v[224:227], v[20:35]
	v_mfma_f32_32x32x16_bf16 v[4:19], v[160:163], v[224:227], v[4:19]
	s_waitcnt lgkmcnt(0)
	v_mfma_f32_32x32x16_bf16 v[20:35], v[96:99], v[228:231], v[20:35]
	v_mfma_f32_32x32x16_bf16 v[4:19], v[164:167], v[228:231], v[4:19]
	s_nop 10
	v_cvt_pk_bf16_f32 v20, v20, v21
	v_cvt_pk_bf16_f32 v21, v22, v23
	v_cvt_pk_bf16_f32 v22, v24, v25
	v_lshl_add_u64 v[24:25], v[196:197], 4, v[188:189]
	v_cvt_pk_bf16_f32 v23, v26, v27
	v_permlane32_swap_b32_e32 v20, v22
	v_cvt_pk_bf16_f32 v4, v4, v5
	v_cvt_pk_bf16_f32 v5, v6, v7
	v_cvt_pk_bf16_f32 v6, v8, v9
	v_cvt_pk_bf16_f32 v7, v10, v11
	v_add_co_u32_e32 v8, vcc, s25, v24
	v_permlane32_swap_b32_e32 v21, v23
	v_permlane32_swap_b32_e32 v4, v6
	v_permlane32_swap_b32_e32 v5, v7
	v_addc_co_u32_e32 v9, vcc, 0, v25, vcc
	global_store_dwordx4 v[24:25], v[20:23], off sc0 sc1 nt
	global_store_dwordx4 v[8:9], v[4:7], off sc0 sc1 nt
	s_and_b64 vcc, exec, s[38:39]
	v_cvt_pk_bf16_f32 v20, v28, v29
	v_cvt_pk_bf16_f32 v21, v30, v31
	v_cvt_pk_bf16_f32 v22, v32, v33
	v_cvt_pk_bf16_f32 v23, v34, v35
	v_cvt_pk_bf16_f32 v4, v12, v13
	v_cvt_pk_bf16_f32 v5, v14, v15
	v_cvt_pk_bf16_f32 v6, v16, v17
	v_cvt_pk_bf16_f32 v7, v18, v19
	v_permlane32_swap_b32_e32 v20, v22
	v_permlane32_swap_b32_e32 v21, v23
	v_permlane32_swap_b32_e32 v4, v6
	v_permlane32_swap_b32_e32 v5, v7
	global_store_dwordx4 v[24:25], v[20:23], off offset:2048 sc0 sc1 nt
	global_store_dwordx4 v[8:9], v[4:7], off offset:2048 sc0 sc1 nt
	s_cbranch_vccz .LBB0_974
	s_xor_b32 s9, s9, 1
	s_and_b64 vcc, exec, s[14:15]
	s_cbranch_vccz .LBB0_970
	s_mul_i32 s4, s9, 0x8400
	v_add_u32_e32 v2, s4, v181
	s_waitcnt vmcnt(7)
	ds_write_b128 v2, v[156:159]
	s_waitcnt vmcnt(6)
	ds_write_b128 v2, v[168:171] offset:8448
	s_waitcnt vmcnt(5)
	ds_write_b128 v2, v[172:175] offset:16896
	s_waitcnt vmcnt(4)
	ds_write_b128 v2, v[176:179] offset:25344
	s_branch .LBB0_970
